# P4 P section: the 8 per-block column-term ds_read_b128 issued up front (one LDS round trip instead of 8)
# baseline (speedup 1.0000x reference)
.LBB0_716:
	v_lshl_add_u32 v141, v151, 2, s83
	ds_read_b32 v143, v141 offset:62720
	v_lshl_add_u32 v196, v122, 2, s83
	ds_read_b128 v[202:205], v196 offset:62208
	ds_read_b128 v[206:209], v196 offset:62272
	ds_read_b128 v[214:217], v196 offset:62336
	ds_read_b128 v[218:221], v196 offset:62400
	ds_read_b128 v[222:225], v196 offset:62464
	ds_read_b128 v[226:229], v196 offset:62528
	ds_read_b128 v[230:233], v196 offset:62592
	ds_read_b128 v[234:237], v196 offset:62656
	s_mov_b64 s[38:39], -1
	s_and_b64 vcc, exec, s[84:85]
	s_cbranch_vccz .LBB0_733
	v_readlane_b32 s38, v243, 31
	v_readlane_b32 s39, v243, 32
	s_waitcnt lgkmcnt(0)
	v_mov_b32_e32 v198, v202
	v_mov_b32_e32 v199, v203
	v_mov_b32_e32 v200, v204
	v_mov_b32_e32 v201, v205
	v_sub_f32_e32 v70, v198, v143
	v_mul_f32_e32 v70, 0x3fb8aa3b, v70
	v_sub_f32_e32 v71, v199, v143
	v_exp_f32_e32 v70, v70
	v_mul_f32_e32 v71, 0x3fb8aa3b, v71
	v_exp_f32_e32 v71, v71
	v_sub_f32_e32 v76, v200, v143
	v_mul_f32_e32 v76, 0x3fb8aa3b, v76
	v_fma_mixlo_f16 v70, v104, v70, 0
	v_exp_f32_e32 v76, v76
	v_sub_f32_e32 v77, v201, v143
	v_cndmask_b32_e64 v70, v70, 0, s[38:39]
	v_readlane_b32 s38, v243, 33
	v_mul_f32_e32 v77, 0x3fb8aa3b, v77
	v_fma_mixlo_f16 v71, v105, v71, 0
	v_readlane_b32 s39, v243, 34
	v_exp_f32_e32 v77, v77
	s_nop 0
	v_cndmask_b32_e64 v71, 0, v71, s[38:39]
	v_readlane_b32 s38, v243, 35
	v_pack_b32_f16 v70, v70, v71
	v_fma_mixlo_f16 v71, v106, v76, 0
	v_readlane_b32 s39, v243, 36
	v_fma_mixlo_f16 v76, v107, v77, 0
	s_nop 0
	v_cndmask_b32_e64 v71, v71, 0, s[38:39]
	v_readlane_b32 s38, v243, 37
	v_readlane_b32 s39, v243, 38
	s_nop 1
	v_cndmask_b32_e64 v76, v76, 0, s[38:39]
	v_pack_b32_f16 v71, v71, v76
	s_cbranch_execz .LBB0_734

.LBB0_719:
	v_readlane_b32 s38, v243, 39
	v_readlane_b32 s39, v243, 40
	s_waitcnt lgkmcnt(0)
	v_mov_b32_e32 v104, v206
	v_mov_b32_e32 v105, v207
	v_mov_b32_e32 v106, v208
	v_mov_b32_e32 v107, v209
	v_sub_f32_e32 v76, v104, v143
	v_sub_f32_e32 v77, v105, v143
	v_mul_f32_e32 v76, 0x3fb8aa3b, v76
	v_mul_f32_e32 v77, 0x3fb8aa3b, v77
	v_exp_f32_e32 v76, v76
	v_exp_f32_e32 v77, v77
	v_sub_f32_e32 v82, v106, v143
	v_mul_f32_e32 v82, 0x3fb8aa3b, v82
	v_fma_mixlo_f16 v72, v72, v76, 0
	v_fma_mixlo_f16 v73, v73, v77, 0
	v_exp_f32_e32 v76, v82
	v_sub_f32_e32 v77, v107, v143
	v_cndmask_b32_e64 v72, v72, 0, s[38:39]
	v_readlane_b32 s38, v243, 41
	v_mul_f32_e32 v77, 0x3fb8aa3b, v77
	v_readlane_b32 s39, v243, 42
	v_exp_f32_e32 v77, v77
	s_nop 0
	v_cndmask_b32_e64 v73, v73, 0, s[38:39]
	v_readlane_b32 s38, v243, 43
	v_pack_b32_f16 v72, v72, v73
	v_fma_mixlo_f16 v73, v74, v76, 0
	v_readlane_b32 s39, v243, 44
	v_fma_mixlo_f16 v74, v75, v77, 0
	s_nop 0
	v_cndmask_b32_e64 v73, v73, 0, s[38:39]
	v_readlane_b32 s38, v243, 45
	v_readlane_b32 s39, v243, 46
	s_nop 1
	v_cndmask_b32_e64 v74, v74, 0, s[38:39]
	v_pack_b32_f16 v73, v73, v74
	s_cbranch_execz .LBB0_736

.LBB0_721:
	v_readlane_b32 s38, v243, 47
	v_readlane_b32 s39, v243, 48
	s_waitcnt lgkmcnt(0)
	v_sub_f32_e32 v74, v214, v143
	v_mul_f32_e32 v74, 0x3fb8aa3b, v74
	v_sub_f32_e32 v75, v215, v143
	v_exp_f32_e32 v74, v74
	v_mul_f32_e32 v75, 0x3fb8aa3b, v75
	v_exp_f32_e32 v75, v75
	v_sub_f32_e32 v76, v216, v143
	v_mul_f32_e32 v76, 0x3fb8aa3b, v76
	v_fma_mixlo_f16 v74, v100, v74, 0
	v_exp_f32_e32 v76, v76
	v_sub_f32_e32 v77, v217, v143
	v_cndmask_b32_e64 v74, v74, 0, s[38:39]
	v_readlane_b32 s38, v243, 49
	v_mul_f32_e32 v77, 0x3fb8aa3b, v77
	v_fma_mixlo_f16 v75, v101, v75, 0
	v_readlane_b32 s39, v243, 50
	v_exp_f32_e32 v77, v77
	s_nop 0
	v_cndmask_b32_e64 v75, v75, 0, s[38:39]
	v_readlane_b32 s38, v243, 51
	v_pack_b32_f16 v74, v74, v75
	v_fma_mixlo_f16 v75, v102, v76, 0
	v_readlane_b32 s39, v243, 52
	v_fma_mixlo_f16 v76, v103, v77, 0
	s_nop 0
	v_cndmask_b32_e64 v75, v75, 0, s[38:39]
	v_readlane_b32 s38, v243, 53
	v_readlane_b32 s39, v243, 54
	s_nop 1
	v_cndmask_b32_e64 v76, v76, 0, s[38:39]
	v_pack_b32_f16 v75, v75, v76
	s_cbranch_execz .LBB0_738

.LBB0_723:
	v_readlane_b32 s0, v243, 55
	v_readlane_b32 s1, v243, 56
	s_waitcnt lgkmcnt(0)
	v_mov_b32_e32 v100, v218
	v_mov_b32_e32 v101, v219
	v_mov_b32_e32 v102, v220
	v_mov_b32_e32 v103, v221
	v_sub_f32_e32 v76, v100, v143
	v_mul_f32_e32 v76, 0x3fb8aa3b, v76
	v_sub_f32_e32 v77, v101, v143
	v_exp_f32_e32 v76, v76
	v_mul_f32_e32 v77, 0x3fb8aa3b, v77
	v_exp_f32_e32 v77, v77
	v_sub_f32_e32 v82, v102, v143
	v_mul_f32_e32 v82, 0x3fb8aa3b, v82
	v_fma_mixlo_f16 v76, v92, v76, 0
	v_exp_f32_e32 v82, v82
	v_sub_f32_e32 v83, v103, v143
	v_cndmask_b32_e64 v76, v76, 0, s[0:1]
	v_readlane_b32 s0, v243, 57
	v_mul_f32_e32 v83, 0x3fb8aa3b, v83
	v_fma_mixlo_f16 v77, v93, v77, 0
	v_readlane_b32 s1, v243, 58
	v_exp_f32_e32 v83, v83
	s_nop 0
	v_cndmask_b32_e64 v77, v77, 0, s[0:1]
	v_readlane_b32 s0, v243, 59
	v_pack_b32_f16 v76, v76, v77
	v_fma_mixlo_f16 v77, v94, v82, 0
	v_readlane_b32 s1, v243, 60
	v_fma_mixlo_f16 v82, v95, v83, 0
	s_nop 0
	v_cndmask_b32_e64 v77, v77, 0, s[0:1]
	v_readlane_b32 s0, v243, 61
	v_readlane_b32 s1, v243, 62
	s_nop 1
	v_cndmask_b32_e64 v82, v82, 0, s[0:1]
	v_pack_b32_f16 v77, v77, v82
	s_cbranch_execz .LBB0_740

.LBB0_725:
	v_readlane_b32 s0, v243, 63
	v_readlane_b32 s1, v242, 0
	s_waitcnt lgkmcnt(0)
	v_mov_b32_e32 v92, v222
	v_mov_b32_e32 v93, v223
	v_mov_b32_e32 v94, v224
	v_mov_b32_e32 v95, v225
	v_sub_f32_e32 v82, v92, v143
	v_mul_f32_e32 v82, 0x3fb8aa3b, v82
	v_sub_f32_e32 v83, v93, v143
	v_exp_f32_e32 v82, v82
	v_mul_f32_e32 v83, 0x3fb8aa3b, v83
	v_exp_f32_e32 v83, v83
	v_sub_f32_e32 v92, v94, v143
	v_mul_f32_e32 v92, 0x3fb8aa3b, v92
	v_fma_mixlo_f16 v82, v96, v82, 0
	v_exp_f32_e32 v92, v92
	v_sub_f32_e32 v93, v95, v143
	v_cndmask_b32_e64 v82, v82, 0, s[0:1]
	v_readlane_b32 s0, v242, 1
	v_mul_f32_e32 v93, 0x3fb8aa3b, v93
	v_fma_mixlo_f16 v83, v97, v83, 0
	v_readlane_b32 s1, v242, 2
	v_exp_f32_e32 v93, v93
	s_nop 0
	v_cndmask_b32_e64 v83, v83, 0, s[0:1]
	v_readlane_b32 s0, v242, 3
	v_pack_b32_f16 v82, v82, v83
	v_fma_mixlo_f16 v83, v98, v92, 0
	v_readlane_b32 s1, v242, 4
	v_fma_mixlo_f16 v92, v99, v93, 0
	s_nop 0
	v_cndmask_b32_e64 v83, v83, 0, s[0:1]
	v_readlane_b32 s0, v242, 5
	v_readlane_b32 s1, v242, 6
	s_nop 1
	v_cndmask_b32_e64 v92, v92, 0, s[0:1]
	v_pack_b32_f16 v83, v83, v92
	s_cbranch_execz .LBB0_742

.LBB0_727:
	s_waitcnt lgkmcnt(0)
	v_mov_b32_e32 v92, v226
	v_mov_b32_e32 v93, v227
	v_mov_b32_e32 v94, v228
	v_mov_b32_e32 v95, v229
	v_sub_f32_e32 v93, v93, v143
	v_mul_f32_e32 v93, 0x3fb8aa3b, v93
	v_sub_f32_e32 v92, v92, v143
	v_exp_f32_e32 v93, v93
	v_mul_f32_e32 v92, 0x3fb8aa3b, v92
	v_exp_f32_e32 v92, v92
	v_sub_f32_e32 v94, v94, v143
	v_fma_mixlo_f16 v85, v85, v93, 0
	v_sub_f32_e32 v93, v95, v143
	v_mul_f32_e32 v94, 0x3fb8aa3b, v94
	v_mul_f32_e32 v93, 0x3fb8aa3b, v93
	v_fma_mixlo_f16 v84, v84, v92, 0
	v_exp_f32_e32 v92, v94
	v_exp_f32_e32 v93, v93
	v_cndmask_b32_e64 v84, v84, 0, s[56:57]
	v_cndmask_b32_e64 v85, v85, 0, s[58:59]
	v_pack_b32_f16 v84, v84, v85
	v_fma_mixlo_f16 v85, v86, v92, 0
	v_fma_mixlo_f16 v86, v87, v93, 0
	v_cndmask_b32_e64 v85, v85, 0, s[60:61]
	v_cndmask_b32_e64 v86, v86, 0, s[62:63]
	v_pack_b32_f16 v85, v85, v86
	s_cbranch_execz .LBB0_744

.LBB0_729:
	s_waitcnt lgkmcnt(0)
	v_mov_b32_e32 v92, v230
	v_mov_b32_e32 v93, v231
	v_mov_b32_e32 v94, v232
	v_mov_b32_e32 v95, v233
	v_sub_f32_e32 v87, v93, v143
	v_mul_f32_e32 v87, 0x3fb8aa3b, v87
	v_sub_f32_e32 v86, v92, v143
	v_exp_f32_e32 v87, v87
	v_mul_f32_e32 v86, 0x3fb8aa3b, v86
	v_exp_f32_e32 v86, v86
	v_sub_f32_e32 v92, v94, v143
	v_fma_mixlo_f16 v87, v89, v87, 0
	v_sub_f32_e32 v89, v95, v143
	v_mul_f32_e32 v92, 0x3fb8aa3b, v92
	v_mul_f32_e32 v89, 0x3fb8aa3b, v89
	v_fma_mixlo_f16 v86, v88, v86, 0
	v_exp_f32_e32 v88, v92
	v_exp_f32_e32 v89, v89
	v_cndmask_b32_e64 v86, v86, 0, s[64:65]
	v_cndmask_b32_e64 v87, v87, 0, s[66:67]
	v_pack_b32_f16 v92, v86, v87
	v_fma_mixlo_f16 v86, v90, v88, 0
	v_fma_mixlo_f16 v87, v91, v89, 0
	v_cndmask_b32_e64 v86, v86, 0, s[68:69]
	v_cndmask_b32_e64 v87, v87, 0, s[70:71]
	v_pack_b32_f16 v93, v86, v87
	s_cbranch_execz .LBB0_746

.LBB0_731:
	s_waitcnt lgkmcnt(0)
	v_mov_b32_e32 v86, v234
	v_mov_b32_e32 v87, v235
	v_mov_b32_e32 v88, v236
	v_mov_b32_e32 v89, v237
	v_sub_f32_e32 v87, v87, v143
	v_mul_f32_e32 v87, 0x3fb8aa3b, v87
	v_sub_f32_e32 v86, v86, v143
	v_exp_f32_e32 v87, v87
	v_mul_f32_e32 v86, 0x3fb8aa3b, v86
	v_exp_f32_e32 v86, v86
	v_sub_f32_e32 v88, v88, v143
	v_fma_mixlo_f16 v79, v79, v87, 0
	v_sub_f32_e32 v87, v89, v143
	v_mul_f32_e32 v88, 0x3fb8aa3b, v88
	v_mul_f32_e32 v87, 0x3fb8aa3b, v87
	v_fma_mixlo_f16 v78, v78, v86, 0
	v_exp_f32_e32 v86, v88
	v_exp_f32_e32 v87, v87
	v_cndmask_b32_e64 v78, v78, 0, s[72:73]
	v_cndmask_b32_e64 v79, v79, 0, s[74:75]
	v_pack_b32_f16 v94, v78, v79
	v_fma_mixlo_f16 v78, v80, v86, 0
	v_fma_mixlo_f16 v79, v81, v87, 0
	v_cndmask_b32_e64 v78, v78, 0, s[76:77]
	v_cndmask_b32_e64 v79, v79, 0, s[78:79]
	v_pack_b32_f16 v95, v78, v79
	s_cbranch_execz .LBB0_748

.LBB0_2116:
	v_lshl_add_u32 v137, v147, 2, s9
	ds_read_b32 v139, v137 offset:62720
	v_lshl_add_u32 v192, v118, 2, s9
	ds_read_b128 v[202:205], v192 offset:62208
	ds_read_b128 v[206:209], v192 offset:62272
	ds_read_b128 v[214:217], v192 offset:62336
	ds_read_b128 v[218:221], v192 offset:62400
	ds_read_b128 v[222:225], v192 offset:62464
	ds_read_b128 v[226:229], v192 offset:62528
	ds_read_b128 v[230:233], v192 offset:62592
	ds_read_b128 v[234:237], v192 offset:62656
	s_mov_b64 s[38:39], -1
	s_and_b64 vcc, exec, s[82:83]
	s_cbranch_vccz .LBB0_2133
	v_readlane_b32 s12, v243, 33
	v_readlane_b32 s13, v243, 34
	s_waitcnt lgkmcnt(0)
	v_mov_b32_e32 v194, v202
	v_mov_b32_e32 v195, v203
	v_mov_b32_e32 v196, v204
	v_mov_b32_e32 v197, v205
	v_sub_f32_e32 v70, v194, v139
	v_sub_f32_e32 v71, v195, v139
	v_mul_f32_e32 v70, 0x3fb8aa3b, v70
	v_mul_f32_e32 v71, 0x3fb8aa3b, v71
	v_exp_f32_e32 v70, v70
	v_exp_f32_e32 v71, v71
	v_sub_f32_e32 v193, v196, v139
	v_mul_f32_e32 v193, 0x3fb8aa3b, v193
	v_fma_mixlo_f16 v70, v100, v70, 0
	v_fma_mixlo_f16 v71, v101, v71, 0
	v_exp_f32_e32 v100, v193
	v_sub_f32_e32 v101, v197, v139
	v_cndmask_b32_e64 v70, v70, 0, s[12:13]
	v_readlane_b32 s12, v243, 35
	v_mul_f32_e32 v101, 0x3fb8aa3b, v101
	v_readlane_b32 s13, v243, 36
	v_exp_f32_e32 v101, v101
	s_nop 0
	v_cndmask_b32_e64 v71, 0, v71, s[12:13]
	v_readlane_b32 s12, v243, 37
	v_pack_b32_f16 v70, v70, v71
	v_fma_mixlo_f16 v71, v102, v100, 0
	v_readlane_b32 s13, v243, 38
	v_fma_mixlo_f16 v100, v103, v101, 0
	s_nop 0
	v_cndmask_b32_e64 v71, v71, 0, s[12:13]
	v_readlane_b32 s12, v243, 39
	v_readlane_b32 s13, v243, 40
	s_nop 1
	v_cndmask_b32_e64 v100, v100, 0, s[12:13]
	v_pack_b32_f16 v71, v71, v100
	s_cbranch_execz .LBB0_2134

.LBB0_2119:
	v_readlane_b32 s12, v243, 41
	v_readlane_b32 s13, v243, 42
	s_waitcnt lgkmcnt(0)
	v_mov_b32_e32 v100, v206
	v_mov_b32_e32 v101, v207
	v_mov_b32_e32 v102, v208
	v_mov_b32_e32 v103, v209
	v_sub_f32_e32 v100, v100, v139
	v_sub_f32_e32 v101, v101, v139
	v_mul_f32_e32 v100, 0x3fb8aa3b, v100
	v_mul_f32_e32 v101, 0x3fb8aa3b, v101
	v_exp_f32_e32 v100, v100
	v_exp_f32_e32 v101, v101
	v_sub_f32_e32 v102, v102, v139
	v_mul_f32_e32 v102, 0x3fb8aa3b, v102
	v_fma_mixlo_f16 v72, v72, v100, 0
	v_fma_mixlo_f16 v73, v73, v101, 0
	v_exp_f32_e32 v100, v102
	v_sub_f32_e32 v101, v103, v139
	v_cndmask_b32_e64 v72, v72, 0, s[12:13]
	v_readlane_b32 s12, v243, 43
	v_mul_f32_e32 v101, 0x3fb8aa3b, v101
	v_readlane_b32 s13, v243, 44
	v_exp_f32_e32 v101, v101
	s_nop 0
	v_cndmask_b32_e64 v73, v73, 0, s[12:13]
	v_readlane_b32 s12, v243, 45
	v_pack_b32_f16 v72, v72, v73
	v_fma_mixlo_f16 v73, v74, v100, 0
	v_readlane_b32 s13, v243, 46
	v_fma_mixlo_f16 v74, v75, v101, 0
	s_nop 0
	v_cndmask_b32_e64 v73, v73, 0, s[12:13]
	v_readlane_b32 s12, v243, 47
	v_readlane_b32 s13, v243, 48
	s_nop 1
	v_cndmask_b32_e64 v74, v74, 0, s[12:13]
	v_pack_b32_f16 v73, v73, v74
	s_cbranch_execz .LBB0_2136

.LBB0_2121:
	v_readlane_b32 s12, v243, 49
	v_readlane_b32 s13, v243, 50
	s_waitcnt lgkmcnt(0)
	v_mov_b32_e32 v100, v214
	v_mov_b32_e32 v101, v215
	v_mov_b32_e32 v102, v216
	v_mov_b32_e32 v103, v217
	v_sub_f32_e32 v74, v100, v139
	v_sub_f32_e32 v75, v101, v139
	v_mul_f32_e32 v74, 0x3fb8aa3b, v74
	v_mul_f32_e32 v75, 0x3fb8aa3b, v75
	v_exp_f32_e32 v74, v74
	v_exp_f32_e32 v75, v75
	v_sub_f32_e32 v100, v102, v139
	v_mul_f32_e32 v100, 0x3fb8aa3b, v100
	v_fma_mixlo_f16 v74, v96, v74, 0
	v_fma_mixlo_f16 v75, v97, v75, 0
	v_exp_f32_e32 v96, v100
	v_sub_f32_e32 v97, v103, v139
	v_cndmask_b32_e64 v74, v74, 0, s[12:13]
	v_readlane_b32 s12, v243, 51
	v_mul_f32_e32 v97, 0x3fb8aa3b, v97
	v_readlane_b32 s13, v243, 52
	v_exp_f32_e32 v97, v97
	s_nop 0
	v_cndmask_b32_e64 v75, v75, 0, s[12:13]
	v_readlane_b32 s12, v243, 53
	v_pack_b32_f16 v74, v74, v75
	v_fma_mixlo_f16 v75, v98, v96, 0
	v_readlane_b32 s13, v243, 54
	v_fma_mixlo_f16 v96, v99, v97, 0
	s_nop 0
	v_cndmask_b32_e64 v75, v75, 0, s[12:13]
	v_readlane_b32 s12, v243, 55
	v_readlane_b32 s13, v243, 56
	s_nop 1
	v_cndmask_b32_e64 v96, v96, 0, s[12:13]
	v_pack_b32_f16 v75, v75, v96
	s_cbranch_execz .LBB0_2138

.LBB0_2123:
	v_readlane_b32 s0, v243, 57
	v_readlane_b32 s1, v243, 58
	s_waitcnt lgkmcnt(0)
	v_mov_b32_e32 v96, v218
	v_mov_b32_e32 v97, v219
	v_mov_b32_e32 v98, v220
	v_mov_b32_e32 v99, v221
	v_sub_f32_e32 v96, v96, v139
	v_sub_f32_e32 v97, v97, v139
	v_mul_f32_e32 v96, 0x3fb8aa3b, v96
	v_mul_f32_e32 v97, 0x3fb8aa3b, v97
	v_exp_f32_e32 v96, v96
	v_exp_f32_e32 v97, v97
	v_sub_f32_e32 v98, v98, v139
	v_mul_f32_e32 v98, 0x3fb8aa3b, v98
	v_fma_mixlo_f16 v76, v76, v96, 0
	v_fma_mixlo_f16 v77, v77, v97, 0
	v_exp_f32_e32 v96, v98
	v_sub_f32_e32 v97, v99, v139
	v_cndmask_b32_e64 v76, v76, 0, s[0:1]
	v_readlane_b32 s0, v243, 59
	v_mul_f32_e32 v97, 0x3fb8aa3b, v97
	v_readlane_b32 s1, v243, 60
	v_exp_f32_e32 v97, v97
	s_nop 0
	v_cndmask_b32_e64 v77, v77, 0, s[0:1]
	v_readlane_b32 s0, v243, 61
	v_pack_b32_f16 v76, v76, v77
	v_fma_mixlo_f16 v77, v78, v96, 0
	v_readlane_b32 s1, v243, 62
	v_fma_mixlo_f16 v78, v79, v97, 0
	s_nop 0
	v_cndmask_b32_e64 v77, v77, 0, s[0:1]
	v_readlane_b32 s0, v243, 63
	v_readlane_b32 s1, v242, 0
	s_nop 1
	v_cndmask_b32_e64 v78, v78, 0, s[0:1]
	v_pack_b32_f16 v77, v77, v78
	s_cbranch_execz .LBB0_2140

.LBB0_2125:
	v_readlane_b32 s0, v242, 1
	v_readlane_b32 s1, v242, 2
	s_waitcnt lgkmcnt(0)
	v_mov_b32_e32 v96, v222
	v_mov_b32_e32 v97, v223
	v_mov_b32_e32 v98, v224
	v_mov_b32_e32 v99, v225
	v_sub_f32_e32 v78, v96, v139
	v_sub_f32_e32 v79, v97, v139
	v_mul_f32_e32 v78, 0x3fb8aa3b, v78
	v_mul_f32_e32 v79, 0x3fb8aa3b, v79
	v_exp_f32_e32 v78, v78
	v_exp_f32_e32 v79, v79
	v_sub_f32_e32 v96, v98, v139
	v_mul_f32_e32 v96, 0x3fb8aa3b, v96
	v_fma_mixlo_f16 v78, v92, v78, 0
	v_fma_mixlo_f16 v79, v93, v79, 0
	v_exp_f32_e32 v92, v96
	v_sub_f32_e32 v93, v99, v139
	v_cndmask_b32_e64 v78, v78, 0, s[0:1]
	v_readlane_b32 s0, v242, 3
	v_mul_f32_e32 v93, 0x3fb8aa3b, v93
	v_readlane_b32 s1, v242, 4
	v_exp_f32_e32 v93, v93
	s_nop 0
	v_cndmask_b32_e64 v79, v79, 0, s[0:1]
	v_readlane_b32 s0, v242, 5
	v_pack_b32_f16 v78, v78, v79
	v_fma_mixlo_f16 v79, v94, v92, 0
	v_readlane_b32 s1, v242, 6
	v_fma_mixlo_f16 v92, v95, v93, 0
	s_nop 0
	v_cndmask_b32_e64 v79, v79, 0, s[0:1]
	v_readlane_b32 s0, v242, 11
	v_readlane_b32 s1, v242, 12
	s_nop 1
	v_cndmask_b32_e64 v92, v92, 0, s[0:1]
	v_pack_b32_f16 v79, v79, v92
	s_cbranch_execz .LBB0_2142

.LBB0_2127:
	v_readlane_b32 s0, v242, 36
	v_readlane_b32 s1, v242, 37
	s_waitcnt lgkmcnt(0)
	v_mov_b32_e32 v92, v226
	v_mov_b32_e32 v93, v227
	v_mov_b32_e32 v94, v228
	v_mov_b32_e32 v95, v229
	v_sub_f32_e32 v93, v93, v139
	v_mul_f32_e32 v93, 0x3fb8aa3b, v93
	v_sub_f32_e32 v92, v92, v139
	v_exp_f32_e32 v93, v93
	v_mul_f32_e32 v92, 0x3fb8aa3b, v92
	v_exp_f32_e32 v92, v92
	v_sub_f32_e32 v94, v94, v139
	v_fma_mixlo_f16 v81, v81, v93, 0
	v_sub_f32_e32 v93, v95, v139
	v_mul_f32_e32 v94, 0x3fb8aa3b, v94
	v_mul_f32_e32 v93, 0x3fb8aa3b, v93
	v_fma_mixlo_f16 v80, v80, v92, 0
	v_exp_f32_e32 v92, v94
	v_exp_f32_e32 v93, v93
	v_cndmask_b32_e64 v80, v80, 0, s[0:1]
	v_readlane_b32 s0, v242, 7
	v_readlane_b32 s1, v242, 8
	s_nop 1
	v_cndmask_b32_e64 v81, v81, 0, s[0:1]
	v_pack_b32_f16 v80, v80, v81
	v_fma_mixlo_f16 v81, v82, v92, 0
	v_fma_mixlo_f16 v82, v83, v93, 0
	v_cndmask_b32_e64 v81, v81, 0, s[60:61]
	v_cndmask_b32_e64 v82, v82, 0, s[62:63]
	v_pack_b32_f16 v81, v81, v82
	s_cbranch_execz .LBB0_2144

.LBB0_2129:
	s_waitcnt lgkmcnt(0)
	v_mov_b32_e32 v92, v230
	v_mov_b32_e32 v93, v231
	v_mov_b32_e32 v94, v232
	v_mov_b32_e32 v95, v233
	v_sub_f32_e32 v83, v93, v139
	v_mul_f32_e32 v83, 0x3fb8aa3b, v83
	v_sub_f32_e32 v82, v92, v139
	v_exp_f32_e32 v83, v83
	v_mul_f32_e32 v82, 0x3fb8aa3b, v82
	v_exp_f32_e32 v82, v82
	v_sub_f32_e32 v92, v94, v139
	v_fma_mixlo_f16 v83, v89, v83, 0
	v_sub_f32_e32 v89, v95, v139
	v_mul_f32_e32 v92, 0x3fb8aa3b, v92
	v_mul_f32_e32 v89, 0x3fb8aa3b, v89
	v_fma_mixlo_f16 v82, v88, v82, 0
	v_exp_f32_e32 v88, v92
	v_exp_f32_e32 v89, v89
	v_cndmask_b32_e64 v82, v82, 0, s[64:65]
	v_cndmask_b32_e64 v83, v83, 0, s[66:67]
	v_pack_b32_f16 v82, v82, v83
	v_fma_mixlo_f16 v83, v90, v88, 0
	v_fma_mixlo_f16 v88, v91, v89, 0
	v_cndmask_b32_e64 v83, v83, 0, s[68:69]
	v_cndmask_b32_e64 v88, v88, 0, s[70:71]
	v_pack_b32_f16 v83, v83, v88
	s_cbranch_execz .LBB0_2146

.LBB0_2131:
	s_waitcnt lgkmcnt(0)
	v_mov_b32_e32 v88, v234
	v_mov_b32_e32 v89, v235
	v_mov_b32_e32 v90, v236
	v_mov_b32_e32 v91, v237
	v_sub_f32_e32 v89, v89, v139
	v_mul_f32_e32 v89, 0x3fb8aa3b, v89
	v_sub_f32_e32 v88, v88, v139
	v_exp_f32_e32 v89, v89
	v_mul_f32_e32 v88, 0x3fb8aa3b, v88
	v_exp_f32_e32 v88, v88
	v_sub_f32_e32 v90, v90, v139
	v_fma_mixlo_f16 v85, v85, v89, 0
	v_sub_f32_e32 v89, v91, v139
	v_mul_f32_e32 v90, 0x3fb8aa3b, v90
	v_mul_f32_e32 v89, 0x3fb8aa3b, v89
	v_fma_mixlo_f16 v84, v84, v88, 0
	v_exp_f32_e32 v88, v90
	v_exp_f32_e32 v89, v89
	v_cndmask_b32_e64 v84, v84, 0, s[72:73]
	v_cndmask_b32_e64 v85, v85, 0, s[74:75]
	v_pack_b32_f16 v84, v84, v85
	v_fma_mixlo_f16 v85, v86, v88, 0
	v_fma_mixlo_f16 v86, v87, v89, 0
	v_cndmask_b32_e64 v85, v85, 0, s[76:77]
	v_cndmask_b32_e64 v86, v86, 0, s[78:79]
	v_pack_b32_f16 v85, v85, v86
	s_cbranch_execz .LBB0_2148

.LBB0_3733:
	v_lshl_add_u32 v137, v147, 2, s83
	ds_read_b32 v139, v137 offset:62720
	v_lshl_add_u32 v192, v118, 2, s83
	ds_read_b128 v[202:205], v192 offset:62208
	ds_read_b128 v[206:209], v192 offset:62272
	ds_read_b128 v[214:217], v192 offset:62336
	ds_read_b128 v[218:221], v192 offset:62400
	ds_read_b128 v[222:225], v192 offset:62464
	ds_read_b128 v[226:229], v192 offset:62528
	ds_read_b128 v[230:233], v192 offset:62592
	ds_read_b128 v[234:237], v192 offset:62656
	s_mov_b64 s[38:39], -1
	s_and_b64 vcc, exec, s[84:85]
	s_cbranch_vccz .LBB0_3750
	v_readlane_b32 s38, v243, 31
	v_readlane_b32 s39, v243, 32
	s_waitcnt lgkmcnt(0)
	v_mov_b32_e32 v194, v202
	v_mov_b32_e32 v195, v203
	v_mov_b32_e32 v196, v204
	v_mov_b32_e32 v197, v205
	v_sub_f32_e32 v70, v194, v139
	v_sub_f32_e32 v71, v195, v139
	v_mul_f32_e32 v70, 0x3fb8aa3b, v70
	v_mul_f32_e32 v71, 0x3fb8aa3b, v71
	v_exp_f32_e32 v70, v70
	v_exp_f32_e32 v71, v71
	v_sub_f32_e32 v193, v196, v139
	v_mul_f32_e32 v193, 0x3fb8aa3b, v193
	v_fma_mixlo_f16 v70, v100, v70, 0
	v_fma_mixlo_f16 v71, v101, v71, 0
	v_exp_f32_e32 v100, v193
	v_sub_f32_e32 v101, v197, v139
	v_cndmask_b32_e64 v70, v70, 0, s[38:39]
	v_readlane_b32 s38, v243, 33
	v_mul_f32_e32 v101, 0x3fb8aa3b, v101
	v_readlane_b32 s39, v243, 34
	v_exp_f32_e32 v101, v101
	s_nop 0
	v_cndmask_b32_e64 v71, 0, v71, s[38:39]
	v_readlane_b32 s38, v243, 35
	v_pack_b32_f16 v70, v70, v71
	v_fma_mixlo_f16 v71, v102, v100, 0
	v_readlane_b32 s39, v243, 36
	v_fma_mixlo_f16 v100, v103, v101, 0
	s_nop 0
	v_cndmask_b32_e64 v71, v71, 0, s[38:39]
	v_readlane_b32 s38, v243, 37
	v_readlane_b32 s39, v243, 38
	s_nop 1
	v_cndmask_b32_e64 v100, v100, 0, s[38:39]
	v_pack_b32_f16 v71, v71, v100
	s_cbranch_execz .LBB0_3751

.LBB0_3736:
	v_readlane_b32 s0, v243, 39
	v_readlane_b32 s1, v243, 40
	s_waitcnt lgkmcnt(0)
	v_mov_b32_e32 v100, v206
	v_mov_b32_e32 v101, v207
	v_mov_b32_e32 v102, v208
	v_mov_b32_e32 v103, v209
	v_sub_f32_e32 v100, v100, v139
	v_sub_f32_e32 v101, v101, v139
	v_mul_f32_e32 v100, 0x3fb8aa3b, v100
	v_mul_f32_e32 v101, 0x3fb8aa3b, v101
	v_exp_f32_e32 v100, v100
	v_exp_f32_e32 v101, v101
	v_sub_f32_e32 v102, v102, v139
	v_mul_f32_e32 v102, 0x3fb8aa3b, v102
	v_fma_mixlo_f16 v72, v72, v100, 0
	v_fma_mixlo_f16 v73, v73, v101, 0
	v_exp_f32_e32 v100, v102
	v_sub_f32_e32 v101, v103, v139
	v_cndmask_b32_e64 v72, v72, 0, s[0:1]
	v_readlane_b32 s0, v243, 41
	v_mul_f32_e32 v101, 0x3fb8aa3b, v101
	v_readlane_b32 s1, v243, 42
	v_exp_f32_e32 v101, v101
	s_nop 0
	v_cndmask_b32_e64 v73, v73, 0, s[0:1]
	v_readlane_b32 s0, v243, 43
	v_pack_b32_f16 v72, v72, v73
	v_fma_mixlo_f16 v73, v74, v100, 0
	v_readlane_b32 s1, v243, 44
	v_fma_mixlo_f16 v74, v75, v101, 0
	s_nop 0
	v_cndmask_b32_e64 v73, v73, 0, s[0:1]
	v_readlane_b32 s0, v243, 45
	v_readlane_b32 s1, v243, 46
	s_nop 1
	v_cndmask_b32_e64 v74, v74, 0, s[0:1]
	v_pack_b32_f16 v73, v73, v74
	s_cbranch_execz .LBB0_3753

.LBB0_3738:
	v_readlane_b32 s0, v243, 47
	v_readlane_b32 s1, v243, 48
	s_waitcnt lgkmcnt(0)
	v_mov_b32_e32 v100, v214
	v_mov_b32_e32 v101, v215
	v_mov_b32_e32 v102, v216
	v_mov_b32_e32 v103, v217
	v_sub_f32_e32 v74, v100, v139
	v_sub_f32_e32 v75, v101, v139
	v_mul_f32_e32 v74, 0x3fb8aa3b, v74
	v_mul_f32_e32 v75, 0x3fb8aa3b, v75
	v_exp_f32_e32 v74, v74
	v_exp_f32_e32 v75, v75
	v_sub_f32_e32 v100, v102, v139
	v_mul_f32_e32 v100, 0x3fb8aa3b, v100
	v_fma_mixlo_f16 v74, v96, v74, 0
	v_fma_mixlo_f16 v75, v97, v75, 0
	v_exp_f32_e32 v96, v100
	v_sub_f32_e32 v97, v103, v139
	v_cndmask_b32_e64 v74, v74, 0, s[0:1]
	v_readlane_b32 s0, v243, 49
	v_mul_f32_e32 v97, 0x3fb8aa3b, v97
	v_readlane_b32 s1, v243, 50
	v_exp_f32_e32 v97, v97
	s_nop 0
	v_cndmask_b32_e64 v75, v75, 0, s[0:1]
	v_readlane_b32 s0, v243, 51
	v_pack_b32_f16 v74, v74, v75
	v_fma_mixlo_f16 v75, v98, v96, 0
	v_readlane_b32 s1, v243, 52
	v_fma_mixlo_f16 v96, v99, v97, 0
	s_nop 0
	v_cndmask_b32_e64 v75, v75, 0, s[0:1]
	v_readlane_b32 s0, v243, 53
	v_readlane_b32 s1, v243, 54
	s_nop 1
	v_cndmask_b32_e64 v96, v96, 0, s[0:1]
	v_pack_b32_f16 v75, v75, v96
	s_cbranch_execz .LBB0_3755

.LBB0_3740:
	v_readlane_b32 s0, v243, 55
	v_readlane_b32 s1, v243, 56
	s_waitcnt lgkmcnt(0)
	v_mov_b32_e32 v96, v218
	v_mov_b32_e32 v97, v219
	v_mov_b32_e32 v98, v220
	v_mov_b32_e32 v99, v221
	v_sub_f32_e32 v96, v96, v139
	v_sub_f32_e32 v97, v97, v139
	v_mul_f32_e32 v96, 0x3fb8aa3b, v96
	v_mul_f32_e32 v97, 0x3fb8aa3b, v97
	v_exp_f32_e32 v96, v96
	v_exp_f32_e32 v97, v97
	v_sub_f32_e32 v98, v98, v139
	v_mul_f32_e32 v98, 0x3fb8aa3b, v98
	v_fma_mixlo_f16 v76, v76, v96, 0
	v_fma_mixlo_f16 v77, v77, v97, 0
	v_exp_f32_e32 v96, v98
	v_sub_f32_e32 v97, v99, v139
	v_cndmask_b32_e64 v76, v76, 0, s[0:1]
	v_readlane_b32 s0, v243, 57
	v_mul_f32_e32 v97, 0x3fb8aa3b, v97
	v_readlane_b32 s1, v243, 58
	v_exp_f32_e32 v97, v97
	s_nop 0
	v_cndmask_b32_e64 v77, v77, 0, s[0:1]
	v_readlane_b32 s0, v243, 59
	v_pack_b32_f16 v76, v76, v77
	v_fma_mixlo_f16 v77, v78, v96, 0
	v_readlane_b32 s1, v243, 60
	v_fma_mixlo_f16 v78, v79, v97, 0
	s_nop 0
	v_cndmask_b32_e64 v77, v77, 0, s[0:1]
	v_readlane_b32 s0, v243, 61
	v_readlane_b32 s1, v243, 62
	s_nop 1
	v_cndmask_b32_e64 v78, v78, 0, s[0:1]
	v_pack_b32_f16 v77, v77, v78
	s_cbranch_execz .LBB0_3757

.LBB0_3742:
	v_readlane_b32 s0, v243, 63
	v_readlane_b32 s1, v242, 0
	s_waitcnt lgkmcnt(0)
	v_mov_b32_e32 v96, v222
	v_mov_b32_e32 v97, v223
	v_mov_b32_e32 v98, v224
	v_mov_b32_e32 v99, v225
	v_sub_f32_e32 v78, v96, v139
	v_sub_f32_e32 v79, v97, v139
	v_mul_f32_e32 v78, 0x3fb8aa3b, v78
	v_mul_f32_e32 v79, 0x3fb8aa3b, v79
	v_exp_f32_e32 v78, v78
	v_exp_f32_e32 v79, v79
	v_sub_f32_e32 v96, v98, v139
	v_mul_f32_e32 v96, 0x3fb8aa3b, v96
	v_fma_mixlo_f16 v78, v92, v78, 0
	v_fma_mixlo_f16 v79, v93, v79, 0
	v_exp_f32_e32 v92, v96
	v_sub_f32_e32 v93, v99, v139
	v_cndmask_b32_e64 v78, v78, 0, s[0:1]
	v_readlane_b32 s0, v242, 1
	v_mul_f32_e32 v93, 0x3fb8aa3b, v93
	v_readlane_b32 s1, v242, 2
	v_exp_f32_e32 v93, v93
	s_nop 0
	v_cndmask_b32_e64 v79, v79, 0, s[0:1]
	v_readlane_b32 s0, v242, 3
	v_pack_b32_f16 v78, v78, v79
	v_fma_mixlo_f16 v79, v94, v92, 0
	v_readlane_b32 s1, v242, 4
	v_fma_mixlo_f16 v92, v95, v93, 0
	s_nop 0
	v_cndmask_b32_e64 v79, v79, 0, s[0:1]
	v_readlane_b32 s0, v242, 5
	v_readlane_b32 s1, v242, 6
	s_nop 1
	v_cndmask_b32_e64 v92, v92, 0, s[0:1]
	v_pack_b32_f16 v79, v79, v92
	s_cbranch_execz .LBB0_3759

.LBB0_3744:
	v_readlane_b32 s0, v242, 11
	v_readlane_b32 s1, v242, 12
	s_waitcnt lgkmcnt(0)
	v_mov_b32_e32 v92, v226
	v_mov_b32_e32 v93, v227
	v_mov_b32_e32 v94, v228
	v_mov_b32_e32 v95, v229
	v_sub_f32_e32 v93, v93, v139
	v_mul_f32_e32 v93, 0x3fb8aa3b, v93
	v_sub_f32_e32 v92, v92, v139
	v_exp_f32_e32 v93, v93
	v_mul_f32_e32 v92, 0x3fb8aa3b, v92
	v_exp_f32_e32 v92, v92
	v_sub_f32_e32 v94, v94, v139
	v_fma_mixlo_f16 v81, v81, v93, 0
	v_sub_f32_e32 v93, v95, v139
	v_mul_f32_e32 v94, 0x3fb8aa3b, v94
	v_mul_f32_e32 v93, 0x3fb8aa3b, v93
	v_fma_mixlo_f16 v80, v80, v92, 0
	v_exp_f32_e32 v92, v94
	v_exp_f32_e32 v93, v93
	v_cndmask_b32_e64 v80, v80, 0, s[0:1]
	v_cndmask_b32_e64 v81, v81, 0, s[58:59]
	v_pack_b32_f16 v80, v80, v81
	v_fma_mixlo_f16 v81, v82, v92, 0
	v_fma_mixlo_f16 v82, v83, v93, 0
	v_cndmask_b32_e64 v81, v81, 0, s[60:61]
	v_cndmask_b32_e64 v82, v82, 0, s[62:63]
	v_pack_b32_f16 v81, v81, v82
	s_cbranch_execz .LBB0_3761

.LBB0_5096:
	v_lshl_add_u32 v137, v147, 2, s81
	ds_read_b32 v139, v137 offset:62720
	v_lshl_add_u32 v192, v118, 2, s81
	ds_read_b128 v[202:205], v192 offset:62208
	ds_read_b128 v[206:209], v192 offset:62272
	ds_read_b128 v[214:217], v192 offset:62336
	ds_read_b128 v[218:221], v192 offset:62400
	ds_read_b128 v[222:225], v192 offset:62464
	ds_read_b128 v[226:229], v192 offset:62528
	ds_read_b128 v[230:233], v192 offset:62592
	ds_read_b128 v[234:237], v192 offset:62656
	s_mov_b64 s[36:37], -1
	s_and_b64 vcc, exec, s[82:83]
	s_cbranch_vccz .LBB0_5113
	v_readlane_b32 s36, v243, 31
	v_readlane_b32 s37, v243, 32
	s_waitcnt lgkmcnt(0)
	v_mov_b32_e32 v194, v202
	v_mov_b32_e32 v195, v203
	v_mov_b32_e32 v196, v204
	v_mov_b32_e32 v197, v205
	v_sub_f32_e32 v70, v194, v139
	v_sub_f32_e32 v71, v195, v139
	v_mul_f32_e32 v70, 0x3fb8aa3b, v70
	v_mul_f32_e32 v71, 0x3fb8aa3b, v71
	v_exp_f32_e32 v70, v70
	v_exp_f32_e32 v71, v71
	v_sub_f32_e32 v193, v196, v139
	v_mul_f32_e32 v193, 0x3fb8aa3b, v193
	v_fma_mixlo_f16 v70, v100, v70, 0
	v_fma_mixlo_f16 v71, v101, v71, 0
	v_exp_f32_e32 v100, v193
	v_sub_f32_e32 v101, v197, v139
	v_cndmask_b32_e64 v70, v70, 0, s[36:37]
	v_readlane_b32 s36, v243, 33
	v_mul_f32_e32 v101, 0x3fb8aa3b, v101
	v_readlane_b32 s37, v243, 34
	v_exp_f32_e32 v101, v101
	s_nop 0
	v_cndmask_b32_e64 v71, 0, v71, s[36:37]
	v_readlane_b32 s36, v243, 35
	v_pack_b32_f16 v70, v70, v71
	v_fma_mixlo_f16 v71, v102, v100, 0
	v_readlane_b32 s37, v243, 36
	v_fma_mixlo_f16 v100, v103, v101, 0
	s_nop 0
	v_cndmask_b32_e64 v71, v71, 0, s[36:37]
	v_readlane_b32 s36, v243, 37
	v_readlane_b32 s37, v243, 38
	s_nop 1
	v_cndmask_b32_e64 v100, v100, 0, s[36:37]
	v_pack_b32_f16 v71, v71, v100
	s_cbranch_execz .LBB0_5114

.LBB0_5099:
	v_readlane_b32 s36, v243, 39
	v_readlane_b32 s37, v243, 40
	s_waitcnt lgkmcnt(0)
	v_mov_b32_e32 v100, v206
	v_mov_b32_e32 v101, v207
	v_mov_b32_e32 v102, v208
	v_mov_b32_e32 v103, v209
	v_sub_f32_e32 v100, v100, v139
	v_sub_f32_e32 v101, v101, v139
	v_mul_f32_e32 v100, 0x3fb8aa3b, v100
	v_mul_f32_e32 v101, 0x3fb8aa3b, v101
	v_exp_f32_e32 v100, v100
	v_exp_f32_e32 v101, v101
	v_sub_f32_e32 v102, v102, v139
	v_mul_f32_e32 v102, 0x3fb8aa3b, v102
	v_fma_mixlo_f16 v72, v72, v100, 0
	v_fma_mixlo_f16 v73, v73, v101, 0
	v_exp_f32_e32 v100, v102
	v_sub_f32_e32 v101, v103, v139
	v_cndmask_b32_e64 v72, v72, 0, s[36:37]
	v_readlane_b32 s36, v243, 41
	v_mul_f32_e32 v101, 0x3fb8aa3b, v101
	v_readlane_b32 s37, v243, 42
	v_exp_f32_e32 v101, v101
	s_nop 0
	v_cndmask_b32_e64 v73, v73, 0, s[36:37]
	v_readlane_b32 s36, v243, 43
	v_pack_b32_f16 v72, v72, v73
	v_fma_mixlo_f16 v73, v74, v100, 0
	v_readlane_b32 s37, v243, 44
	v_fma_mixlo_f16 v74, v75, v101, 0
	s_nop 0
	v_cndmask_b32_e64 v73, v73, 0, s[36:37]
	v_readlane_b32 s36, v243, 45
	v_readlane_b32 s37, v243, 46
	s_nop 1
	v_cndmask_b32_e64 v74, v74, 0, s[36:37]
	v_pack_b32_f16 v73, v73, v74
	s_cbranch_execz .LBB0_5116

.LBB0_5101:
	v_readlane_b32 s36, v243, 47
	v_readlane_b32 s37, v243, 48
	s_waitcnt lgkmcnt(0)
	v_mov_b32_e32 v100, v214
	v_mov_b32_e32 v101, v215
	v_mov_b32_e32 v102, v216
	v_mov_b32_e32 v103, v217
	v_sub_f32_e32 v74, v100, v139
	v_sub_f32_e32 v75, v101, v139
	v_mul_f32_e32 v74, 0x3fb8aa3b, v74
	v_mul_f32_e32 v75, 0x3fb8aa3b, v75
	v_exp_f32_e32 v74, v74
	v_exp_f32_e32 v75, v75
	v_sub_f32_e32 v100, v102, v139
	v_mul_f32_e32 v100, 0x3fb8aa3b, v100
	v_fma_mixlo_f16 v74, v96, v74, 0
	v_fma_mixlo_f16 v75, v97, v75, 0
	v_exp_f32_e32 v96, v100
	v_sub_f32_e32 v97, v103, v139
	v_cndmask_b32_e64 v74, v74, 0, s[36:37]
	v_readlane_b32 s36, v243, 49
	v_mul_f32_e32 v97, 0x3fb8aa3b, v97
	v_readlane_b32 s37, v243, 50
	v_exp_f32_e32 v97, v97
	s_nop 0
	v_cndmask_b32_e64 v75, v75, 0, s[36:37]
	v_readlane_b32 s36, v243, 51
	v_pack_b32_f16 v74, v74, v75
	v_fma_mixlo_f16 v75, v98, v96, 0
	v_readlane_b32 s37, v243, 52
	v_fma_mixlo_f16 v96, v99, v97, 0
	s_nop 0
	v_cndmask_b32_e64 v75, v75, 0, s[36:37]
	v_readlane_b32 s36, v243, 53
	v_readlane_b32 s37, v243, 54
	s_nop 1
	v_cndmask_b32_e64 v96, v96, 0, s[36:37]
	v_pack_b32_f16 v75, v75, v96
	s_cbranch_execz .LBB0_5118

.LBB0_5103:
	v_readlane_b32 s2, v243, 55
	v_readlane_b32 s3, v243, 56
	s_waitcnt lgkmcnt(0)
	v_mov_b32_e32 v96, v218
	v_mov_b32_e32 v97, v219
	v_mov_b32_e32 v98, v220
	v_mov_b32_e32 v99, v221
	v_sub_f32_e32 v96, v96, v139
	v_sub_f32_e32 v97, v97, v139
	v_mul_f32_e32 v96, 0x3fb8aa3b, v96
	v_mul_f32_e32 v97, 0x3fb8aa3b, v97
	v_exp_f32_e32 v96, v96
	v_exp_f32_e32 v97, v97
	v_sub_f32_e32 v98, v98, v139
	v_mul_f32_e32 v98, 0x3fb8aa3b, v98
	v_fma_mixlo_f16 v76, v76, v96, 0
	v_fma_mixlo_f16 v77, v77, v97, 0
	v_exp_f32_e32 v96, v98
	v_sub_f32_e32 v97, v99, v139
	v_cndmask_b32_e64 v76, v76, 0, s[2:3]
	v_readlane_b32 s2, v243, 57
	v_mul_f32_e32 v97, 0x3fb8aa3b, v97
	v_readlane_b32 s3, v243, 58
	v_exp_f32_e32 v97, v97
	s_nop 0
	v_cndmask_b32_e64 v77, v77, 0, s[2:3]
	v_readlane_b32 s2, v243, 59
	v_pack_b32_f16 v76, v76, v77
	v_fma_mixlo_f16 v77, v78, v96, 0
	v_readlane_b32 s3, v243, 60
	v_fma_mixlo_f16 v78, v79, v97, 0
	s_nop 0
	v_cndmask_b32_e64 v77, v77, 0, s[2:3]
	v_readlane_b32 s2, v243, 61
	v_readlane_b32 s3, v243, 62
	s_nop 1
	v_cndmask_b32_e64 v78, v78, 0, s[2:3]
	v_pack_b32_f16 v77, v77, v78
	s_cbranch_execz .LBB0_5120

.LBB0_5105:
	v_readlane_b32 s2, v243, 63
	v_readlane_b32 s3, v242, 0
	s_waitcnt lgkmcnt(0)
	v_mov_b32_e32 v96, v222
	v_mov_b32_e32 v97, v223
	v_mov_b32_e32 v98, v224
	v_mov_b32_e32 v99, v225
	v_sub_f32_e32 v78, v96, v139
	v_sub_f32_e32 v79, v97, v139
	v_mul_f32_e32 v78, 0x3fb8aa3b, v78
	v_mul_f32_e32 v79, 0x3fb8aa3b, v79
	v_exp_f32_e32 v78, v78
	v_exp_f32_e32 v79, v79
	v_sub_f32_e32 v96, v98, v139
	v_mul_f32_e32 v96, 0x3fb8aa3b, v96
	v_fma_mixlo_f16 v78, v92, v78, 0
	v_fma_mixlo_f16 v79, v93, v79, 0
	v_exp_f32_e32 v92, v96
	v_sub_f32_e32 v93, v99, v139
	v_cndmask_b32_e64 v78, v78, 0, s[2:3]
	v_readlane_b32 s2, v242, 1
	v_mul_f32_e32 v93, 0x3fb8aa3b, v93
	v_readlane_b32 s3, v242, 2
	v_exp_f32_e32 v93, v93
	s_nop 0
	v_cndmask_b32_e64 v79, v79, 0, s[2:3]
	v_readlane_b32 s2, v242, 3
	v_pack_b32_f16 v78, v78, v79
	v_fma_mixlo_f16 v79, v94, v92, 0
	v_readlane_b32 s3, v242, 4
	v_fma_mixlo_f16 v92, v95, v93, 0
	s_nop 0
	v_cndmask_b32_e64 v79, v79, 0, s[2:3]
	v_readlane_b32 s2, v242, 5
	v_readlane_b32 s3, v242, 6
	s_nop 1
	v_cndmask_b32_e64 v92, v92, 0, s[2:3]
	v_pack_b32_f16 v79, v79, v92
	s_cbranch_execz .LBB0_5122

.LBB0_5107:
	v_readlane_b32 s2, v242, 11
	v_readlane_b32 s3, v242, 12
	s_waitcnt lgkmcnt(0)
	v_mov_b32_e32 v92, v226
	v_mov_b32_e32 v93, v227
	v_mov_b32_e32 v94, v228
	v_mov_b32_e32 v95, v229
	v_sub_f32_e32 v93, v93, v139
	v_mul_f32_e32 v93, 0x3fb8aa3b, v93
	v_sub_f32_e32 v92, v92, v139
	v_exp_f32_e32 v93, v93
	v_mul_f32_e32 v92, 0x3fb8aa3b, v92
	v_exp_f32_e32 v92, v92
	v_sub_f32_e32 v94, v94, v139
	v_fma_mixlo_f16 v81, v81, v93, 0
	v_sub_f32_e32 v93, v95, v139
	v_mul_f32_e32 v94, 0x3fb8aa3b, v94
	v_mul_f32_e32 v93, 0x3fb8aa3b, v93
	v_fma_mixlo_f16 v80, v80, v92, 0
	v_exp_f32_e32 v92, v94
	v_exp_f32_e32 v93, v93
	v_cndmask_b32_e64 v80, v80, 0, s[2:3]
	v_cndmask_b32_e64 v81, v81, 0, s[56:57]
	v_pack_b32_f16 v80, v80, v81
	v_fma_mixlo_f16 v81, v82, v92, 0
	v_fma_mixlo_f16 v82, v83, v93, 0
	v_cndmask_b32_e64 v81, v81, 0, s[58:59]
	v_cndmask_b32_e64 v82, v82, 0, s[60:61]
	v_pack_b32_f16 v81, v81, v82
	s_cbranch_execz .LBB0_5124

.LBB0_5109:
	s_waitcnt lgkmcnt(0)
	v_mov_b32_e32 v92, v230
	v_mov_b32_e32 v93, v231
	v_mov_b32_e32 v94, v232
	v_mov_b32_e32 v95, v233
	v_sub_f32_e32 v83, v93, v139
	v_mul_f32_e32 v83, 0x3fb8aa3b, v83
	v_sub_f32_e32 v82, v92, v139
	v_exp_f32_e32 v83, v83
	v_mul_f32_e32 v82, 0x3fb8aa3b, v82
	v_exp_f32_e32 v82, v82
	v_sub_f32_e32 v92, v94, v139
	v_fma_mixlo_f16 v83, v89, v83, 0
	v_sub_f32_e32 v89, v95, v139
	v_mul_f32_e32 v92, 0x3fb8aa3b, v92
	v_mul_f32_e32 v89, 0x3fb8aa3b, v89
	v_fma_mixlo_f16 v82, v88, v82, 0
	v_exp_f32_e32 v88, v92
	v_exp_f32_e32 v89, v89
	v_cndmask_b32_e64 v82, v82, 0, s[62:63]
	v_cndmask_b32_e64 v83, v83, 0, s[64:65]
	v_pack_b32_f16 v82, v82, v83
	v_fma_mixlo_f16 v83, v90, v88, 0
	v_fma_mixlo_f16 v88, v91, v89, 0
	v_cndmask_b32_e64 v83, v83, 0, s[66:67]
	v_cndmask_b32_e64 v88, v88, 0, s[68:69]
	v_pack_b32_f16 v83, v83, v88
	s_cbranch_execz .LBB0_5126

.LBB0_5111:
	s_waitcnt lgkmcnt(0)
	v_mov_b32_e32 v88, v234
	v_mov_b32_e32 v89, v235
	v_mov_b32_e32 v90, v236
	v_mov_b32_e32 v91, v237
	v_sub_f32_e32 v89, v89, v139
	v_mul_f32_e32 v89, 0x3fb8aa3b, v89
	v_sub_f32_e32 v88, v88, v139
	v_exp_f32_e32 v89, v89
	v_mul_f32_e32 v88, 0x3fb8aa3b, v88
	v_exp_f32_e32 v88, v88
	v_sub_f32_e32 v90, v90, v139
	v_fma_mixlo_f16 v85, v85, v89, 0
	v_sub_f32_e32 v89, v91, v139
	v_mul_f32_e32 v90, 0x3fb8aa3b, v90
	v_mul_f32_e32 v89, 0x3fb8aa3b, v89
	v_fma_mixlo_f16 v84, v84, v88, 0
	v_exp_f32_e32 v88, v90
	v_exp_f32_e32 v89, v89
	v_cndmask_b32_e64 v84, v84, 0, s[70:71]
	v_cndmask_b32_e64 v85, v85, 0, s[72:73]
	v_pack_b32_f16 v84, v84, v85
	v_fma_mixlo_f16 v85, v86, v88, 0
	v_fma_mixlo_f16 v86, v87, v89, 0
	v_cndmask_b32_e64 v85, v85, 0, s[74:75]
	v_cndmask_b32_e64 v86, v86, 0, s[76:77]
	v_pack_b32_f16 v85, v85, v86
	s_cbranch_execz .LBB0_5128
